# P5a: waves 4-7 carry second-half MFMAs across the stage barrier (stagger) + epilogue slot loads issued together
# speedup vs baseline: 1.0083x; 1.0083x over previous
;     __device__ __forceinline__ bool desc(int i, Desc& d) const { const int u = blockIdx.x + gridDim.x * i; if (u >= 128) return false; d.mt = u; return true; }
; __device__ __forceinline__ void xmap_find(const XMap& m, int tix, int& lo_out, int& ti) {
;     int lo = 0;
; #pragma unroll
;     for (int step = 16; step >= 1; step >>= 1) if (m.pref[lo + step] <= tix) lo += step;
;     lo_out = lo; ti = tix - m.pref[lo];
; }
;     __device__ __forceinline__ bool desc(int i, Desc& d) const {
;         if (i >= xm.nmine) return false;
;         const int lu = xm.lb + xm.nlb * i; int lo, ti; xmap_find(xm, lu >> 1, lo, ti);
;         d.e = xm.x + 8 * lo; d.jt = lu & 1; d.nrow = xm.cntl[lo] - ti * 256; d.lst = p.lists + (size_t)d.e * NLAT + ti * 256;
;         return true;
.LBB0_1038:
	s_waitcnt lgkmcnt(0)
	s_barrier
	s_cmp_lt_u32 s4, 0x4000
	s_cbranch_scc1 .Lp5a_nodef
	s_cmp_eq_u32 s30, 0
	s_cbranch_scc1 .Lp5a_nodef
	s_cmp_eq_u32 s0, 0
	s_cbranch_scc1 .Lp5a_nodef
	v_mfma_scale_f32_16x16x128_f8f6f4 v[66:69], v[158:165], v[206:213], v[66:69], v178, v178 op_sel_hi:[0,0,0]
	v_mfma_scale_f32_16x16x128_f8f6f4 v[58:61], v[182:189], v[206:213], v[58:61], v178, v178 op_sel_hi:[0,0,0]
	v_mfma_scale_f32_16x16x128_f8f6f4 v[62:65], v[190:197], v[206:213], v[62:65], v178, v178 op_sel_hi:[0,0,0]
	v_mfma_scale_f32_16x16x128_f8f6f4 v[54:57], v[198:205], v[206:213], v[54:57], v178, v178 op_sel_hi:[0,0,0]
	v_mfma_scale_f32_16x16x128_f8f6f4 v[50:53], v[158:165], v[214:221], v[50:53], v178, v178 op_sel_hi:[0,0,0]
	v_mfma_scale_f32_16x16x128_f8f6f4 v[42:45], v[182:189], v[214:221], v[42:45], v178, v178 op_sel_hi:[0,0,0]
	v_mfma_scale_f32_16x16x128_f8f6f4 v[46:49], v[190:197], v[214:221], v[46:49], v178, v178 op_sel_hi:[0,0,0]
	v_mfma_scale_f32_16x16x128_f8f6f4 v[38:41], v[198:205], v[214:221], v[38:41], v178, v178 op_sel_hi:[0,0,0]
	v_mfma_scale_f32_16x16x128_f8f6f4 v[34:37], v[158:165], v[222:229], v[34:37], v178, v178 op_sel_hi:[0,0,0]
	v_mfma_scale_f32_16x16x128_f8f6f4 v[26:29], v[182:189], v[222:229], v[26:29], v178, v178 op_sel_hi:[0,0,0]
	v_mfma_scale_f32_16x16x128_f8f6f4 v[30:33], v[190:197], v[222:229], v[30:33], v178, v178 op_sel_hi:[0,0,0]
	v_mfma_scale_f32_16x16x128_f8f6f4 v[22:25], v[198:205], v[222:229], v[22:25], v178, v178 op_sel_hi:[0,0,0]
	v_mfma_scale_f32_16x16x128_f8f6f4 v[18:21], v[158:165], v[230:237], v[18:21], v178, v178 op_sel_hi:[0,0,0]
	v_mfma_scale_f32_16x16x128_f8f6f4 v[10:13], v[182:189], v[230:237], v[10:13], v178, v178 op_sel_hi:[0,0,0]
	v_mfma_scale_f32_16x16x128_f8f6f4 v[14:17], v[190:197], v[230:237], v[14:17], v178, v178 op_sel_hi:[0,0,0]
	v_mfma_scale_f32_16x16x128_f8f6f4 v[6:9], v[198:205], v[230:237], v[6:9], v178, v178 op_sel_hi:[0,0,0]
.Lp5a_nodef:
	s_andn2_b64 vcc, exec, s[14:15]
	s_cbranch_vccnz .LBB0_1046
	s_lshl_b32 s13, s5, 16
	s_lshl_b32 s14, s9, 6
	s_and_b32 s13, s13, 0x10000
	s_ashr_i32 s15, s14, 31
	s_lshl_b64 s[14:15], s[14:15], 1
	s_add_i32 s13, s4, s13
	v_lshl_add_u64 v[4:5], v[140:141], 0, s[14:15]
	s_mov_b32 m0, s13
	s_add_i32 s9, s9, 1
	global_load_lds_dwordx4 v[4:5], off
	v_lshl_add_u64 v[4:5], v[142:143], 0, s[14:15]
	s_add_i32 m0, s13, 0x400
	s_nop 0
	global_load_lds_dwordx4 v[4:5], off
	v_lshl_add_u64 v[4:5], v[144:145], 0, s[14:15]
	s_add_i32 m0, s13, 0x800
	s_nop 0
	global_load_lds_dwordx4 v[4:5], off
	v_lshl_add_u64 v[4:5], v[146:147], 0, s[14:15]
	s_add_i32 m0, s13, 0xc00
	s_nop 0
	global_load_lds_dwordx4 v[4:5], off
	v_lshl_add_u64 v[4:5], v[148:149], 0, s[14:15]
	s_add_i32 m0, s13, 0x8000
	s_nop 0
	global_load_lds_dwordx4 v[4:5], off
	v_lshl_add_u64 v[4:5], v[150:151], 0, s[14:15]
	s_add_i32 m0, s13, 0x8400
	s_nop 0
	global_load_lds_dwordx4 v[4:5], off
	v_lshl_add_u64 v[4:5], v[152:153], 0, s[14:15]
	s_add_i32 m0, s13, 0x8800
	s_nop 0
	global_load_lds_dwordx4 v[4:5], off
	v_lshl_add_u64 v[4:5], v[154:155], 0, s[14:15]
	s_add_i32 m0, s13, 0x8c00
	s_cmp_lg_u32 s9, 8
	global_load_lds_dwordx4 v[4:5], off
	s_mov_b64 s[14:15], -1
	s_cbranch_scc1 .LBB0_1049
	s_andn2_b64 vcc, exec, s[10:11]
	s_cbranch_vccnz .LBB0_1047
	s_add_i32 s9, s41, 2
	s_cmp_lt_i32 s9, s3
	v_mov_b32_e32 v139, v0
	v_mov_b32_e32 v138, v0
	s_cselect_b64 s[12:13], -1, 0
	s_cmp_ge_i32 s9, s3
	v_mov_b64_e32 v[4:5], v[134:135]
	v_mov_b32_e32 v158, v168
	s_mov_b32 s16, s8
	v_mov_b32_e32 v159, v136
	s_cbranch_scc1 .LBB0_1043
	ds_read_b32 v2, v177
	s_mul_i32 s9, s9, s64
	s_add_i32 s9, s9, s69
	s_ashr_i32 s10, s9, 1
	s_and_b32 s16, s9, 1
	s_waitcnt lgkmcnt(0)
	v_cmp_lt_i32_e32 vcc, s10, v2
	s_nop 1
	v_cndmask_b32_e64 v2, 16, 0, vcc
	v_or_b32_e32 v4, 8, v2
	v_lshlrev_b32_e32 v5, 2, v4
	v_or_b32_e32 v5, 0x20000, v5
	ds_read_b32 v5, v5
	s_waitcnt lgkmcnt(0)
	v_cmp_lt_i32_e32 vcc, s10, v5
	s_nop 1
	v_cndmask_b32_e32 v2, v4, v2, vcc
	v_or_b32_e32 v4, 4, v2
	v_lshlrev_b32_e32 v5, 2, v4
	v_or_b32_e32 v5, 0x20000, v5
	ds_read_b32 v5, v5
	s_waitcnt lgkmcnt(0)
	v_cmp_lt_i32_e32 vcc, s10, v5
	s_nop 1
	v_cndmask_b32_e32 v2, v4, v2, vcc
	v_or_b32_e32 v4, 2, v2
	v_lshlrev_b32_e32 v5, 2, v4
	v_add_u32_e32 v5, 0x20000, v5
	ds_read_b32 v5, v5
	s_waitcnt lgkmcnt(0)
	v_cmp_lt_i32_e32 vcc, s10, v5
	s_nop 1
	v_cndmask_b32_e32 v2, v4, v2, vcc
	v_add_u32_e32 v4, 1, v2
	v_lshlrev_b32_e32 v5, 2, v4
	v_add_u32_e32 v5, 0x20000, v5
	ds_read_b32 v5, v5
	s_waitcnt lgkmcnt(0)
	v_cmp_lt_i32_e32 vcc, s10, v5
	s_nop 1
	v_cndmask_b32_e32 v2, v4, v2, vcc
	v_lshlrev_b32_e32 v4, 2, v2
	v_add_u32_e32 v5, 0x20000, v4
	ds_read_b32 v140, v5
	v_add_u32_e32 v4, 0x20100, v4
	ds_read_b32 v141, v4
	v_lshlrev_b32_e32 v2, 3, v2
	v_or_b32_e32 v2, s68, v2
	s_waitcnt lgkmcnt(0)
	v_sub_u32_e32 v140, s10, v140
	v_lshlrev_b32_e32 v140, 8, v140
	v_lshlrev_b64 v[4:5], 17, v[2:3]
	v_sub_u32_e32 v158, v141, v140
	v_ashrrev_i32_e32 v141, 31, v140
	v_lshl_add_u64 v[4:5], s[52:53], 0, v[4:5]
	v_lshlrev_b64 v[140:141], 2, v[140:141]
	v_lshl_add_u64 v[4:5], v[4:5], 0, v[140:141]
	v_mov_b32_e32 v159, v2

.LBB0_1050:
	s_cmp_lt_u32 s4, 0x4000
	s_cbranch_scc0 .Lp5a_ybody
	s_and_b32 s13, s31, 0x10000
	v_add_u32_e32 v2, s13, v249
	v_xor_b32_e32 v4, 64, v2
	v_or_b32_e32 v5, s13, v250
	v_xor_b32_e32 v166, 64, v5
	ds_read_b128 v[158:161], v5 offset:0
	ds_read_b128 v[162:165], v166 offset:0
	ds_read_b128 v[182:185], v5 offset:0x800
	ds_read_b128 v[186:189], v166 offset:0x800
	ds_read_b128 v[190:193], v5 offset:0x1000
	ds_read_b128 v[194:197], v166 offset:0x1000
	ds_read_b128 v[198:201], v5 offset:0x1800
	ds_read_b128 v[202:205], v166 offset:0x1800
	ds_read_b128 v[206:209], v2 offset:0
	ds_read_b128 v[210:213], v4 offset:0
	ds_read_b128 v[214:217], v2 offset:0x800
	ds_read_b128 v[218:221], v4 offset:0x800
	ds_read_b128 v[222:225], v2 offset:0x1000
	ds_read_b128 v[226:229], v4 offset:0x1000
	ds_read_b128 v[230:233], v2 offset:0x1800
	ds_read_b128 v[234:237], v4 offset:0x1800
	s_waitcnt lgkmcnt(4)
	s_nop 0
	v_mfma_scale_f32_16x16x128_f8f6f4 v[130:133], v[158:165], v[206:213], v[130:133], v178, v178 op_sel_hi:[0,0,0]
	v_mfma_scale_f32_16x16x128_f8f6f4 v[122:125], v[182:189], v[206:213], v[122:125], v178, v178 op_sel_hi:[0,0,0]
	v_mfma_scale_f32_16x16x128_f8f6f4 v[126:129], v[190:197], v[206:213], v[126:129], v178, v178 op_sel_hi:[0,0,0]
	v_mfma_scale_f32_16x16x128_f8f6f4 v[118:121], v[198:205], v[206:213], v[118:121], v178, v178 op_sel_hi:[0,0,0]
	v_mfma_scale_f32_16x16x128_f8f6f4 v[114:117], v[158:165], v[214:221], v[114:117], v178, v178 op_sel_hi:[0,0,0]
	v_mfma_scale_f32_16x16x128_f8f6f4 v[106:109], v[182:189], v[214:221], v[106:109], v178, v178 op_sel_hi:[0,0,0]
	v_mfma_scale_f32_16x16x128_f8f6f4 v[110:113], v[190:197], v[214:221], v[110:113], v178, v178 op_sel_hi:[0,0,0]
	v_mfma_scale_f32_16x16x128_f8f6f4 v[102:105], v[198:205], v[214:221], v[102:105], v178, v178 op_sel_hi:[0,0,0]
	ds_read_b128 v[206:209], v2 offset:0x2000
	ds_read_b128 v[210:213], v4 offset:0x2000
	ds_read_b128 v[214:217], v2 offset:0x2800
	ds_read_b128 v[218:221], v4 offset:0x2800
	s_waitcnt lgkmcnt(4)
	v_mfma_scale_f32_16x16x128_f8f6f4 v[98:101], v[158:165], v[222:229], v[98:101], v178, v178 op_sel_hi:[0,0,0]
	v_mfma_scale_f32_16x16x128_f8f6f4 v[90:93], v[182:189], v[222:229], v[90:93], v178, v178 op_sel_hi:[0,0,0]
	v_mfma_scale_f32_16x16x128_f8f6f4 v[94:97], v[190:197], v[222:229], v[94:97], v178, v178 op_sel_hi:[0,0,0]
	v_mfma_scale_f32_16x16x128_f8f6f4 v[86:89], v[198:205], v[222:229], v[86:89], v178, v178 op_sel_hi:[0,0,0]
	v_mfma_scale_f32_16x16x128_f8f6f4 v[82:85], v[158:165], v[230:237], v[82:85], v178, v178 op_sel_hi:[0,0,0]
	v_mfma_scale_f32_16x16x128_f8f6f4 v[74:77], v[182:189], v[230:237], v[74:77], v178, v178 op_sel_hi:[0,0,0]
	v_mfma_scale_f32_16x16x128_f8f6f4 v[78:81], v[190:197], v[230:237], v[78:81], v178, v178 op_sel_hi:[0,0,0]
	v_mfma_scale_f32_16x16x128_f8f6f4 v[70:73], v[198:205], v[230:237], v[70:73], v178, v178 op_sel_hi:[0,0,0]
	ds_read_b128 v[222:225], v2 offset:0x3000
	ds_read_b128 v[226:229], v4 offset:0x3000
	ds_read_b128 v[230:233], v2 offset:0x3800
	ds_read_b128 v[234:237], v4 offset:0x3800
	s_waitcnt lgkmcnt(4)
	v_mfma_scale_f32_16x16x128_f8f6f4 v[66:69], v[158:165], v[206:213], v[66:69], v178, v178 op_sel_hi:[0,0,0]
	v_mfma_scale_f32_16x16x128_f8f6f4 v[58:61], v[182:189], v[206:213], v[58:61], v178, v178 op_sel_hi:[0,0,0]
	v_mfma_scale_f32_16x16x128_f8f6f4 v[62:65], v[190:197], v[206:213], v[62:65], v178, v178 op_sel_hi:[0,0,0]
	v_mfma_scale_f32_16x16x128_f8f6f4 v[54:57], v[198:205], v[206:213], v[54:57], v178, v178 op_sel_hi:[0,0,0]
	v_mfma_scale_f32_16x16x128_f8f6f4 v[50:53], v[158:165], v[214:221], v[50:53], v178, v178 op_sel_hi:[0,0,0]
	v_mfma_scale_f32_16x16x128_f8f6f4 v[42:45], v[182:189], v[214:221], v[42:45], v178, v178 op_sel_hi:[0,0,0]
	v_mfma_scale_f32_16x16x128_f8f6f4 v[46:49], v[190:197], v[214:221], v[46:49], v178, v178 op_sel_hi:[0,0,0]
	v_mfma_scale_f32_16x16x128_f8f6f4 v[38:41], v[198:205], v[214:221], v[38:41], v178, v178 op_sel_hi:[0,0,0]
	s_waitcnt lgkmcnt(0)
	v_mfma_scale_f32_16x16x128_f8f6f4 v[34:37], v[158:165], v[222:229], v[34:37], v178, v178 op_sel_hi:[0,0,0]
	v_mfma_scale_f32_16x16x128_f8f6f4 v[26:29], v[182:189], v[222:229], v[26:29], v178, v178 op_sel_hi:[0,0,0]
	v_mfma_scale_f32_16x16x128_f8f6f4 v[30:33], v[190:197], v[222:229], v[30:33], v178, v178 op_sel_hi:[0,0,0]
	v_mfma_scale_f32_16x16x128_f8f6f4 v[22:25], v[198:205], v[222:229], v[22:25], v178, v178 op_sel_hi:[0,0,0]
	v_mfma_scale_f32_16x16x128_f8f6f4 v[18:21], v[158:165], v[230:237], v[18:21], v178, v178 op_sel_hi:[0,0,0]
	v_mfma_scale_f32_16x16x128_f8f6f4 v[10:13], v[182:189], v[230:237], v[10:13], v178, v178 op_sel_hi:[0,0,0]
	v_mfma_scale_f32_16x16x128_f8f6f4 v[14:17], v[190:197], v[230:237], v[14:17], v178, v178 op_sel_hi:[0,0,0]
	v_mfma_scale_f32_16x16x128_f8f6f4 v[6:9], v[198:205], v[230:237], v[6:9], v178, v178 op_sel_hi:[0,0,0]
	s_branch .LBB0_1032
; #define GS_WAIT(ahead) do { if ((ahead) >= 1) asm volatile("s_waitcnt vmcnt(8)" ::: "memory"); else asm volatile("s_waitcnt vmcnt(0)" ::: "memory"); } while (0)
; #define GS_WAIT(ahead) do { if ((ahead) >= 2) asm volatile("s_waitcnt vmcnt(8)" ::: "memory"); else if ((ahead) == 1) asm volatile("s_waitcnt vmcnt(4)" ::: "memory"); \
;         else asm volatile("s_waitcnt vmcnt(0)" ::: "memory"); } while (0)
; template <class PH>
; __device__ __forceinline__ void gemm_stream(unsigned char* smem, PH& ph) {
;     ...
;         if (computed < issued) { GS_WAIT(0); prewaited = true; }
;         asm volatile("s_waitcnt lgkmcnt(0)" ::: "memory"); __builtin_amdgcn_s_barrier(); asm volatile("" ::: "memory");
;         ph.epilogue(acc, d_cmp, smem + ((computed + 1) & 1) * 65536 + wid * STG_WAVE);
.Lp5a_ybody:
	s_and_b32 s13, s31, 0x10000
	v_add_u32_e32 v2, s13, v249
	v_xor_b32_e32 v4, 64, v2
	v_or_b32_e32 v5, s13, v250
	v_xor_b32_e32 v166, 64, v5
	ds_read_b128 v[158:161], v5 offset:0
	ds_read_b128 v[162:165], v166 offset:0
	ds_read_b128 v[182:185], v5 offset:0x800
	ds_read_b128 v[186:189], v166 offset:0x800
	ds_read_b128 v[190:193], v5 offset:0x1000
	ds_read_b128 v[194:197], v166 offset:0x1000
	ds_read_b128 v[198:201], v5 offset:0x1800
	ds_read_b128 v[202:205], v166 offset:0x1800
	ds_read_b128 v[206:209], v2 offset:0
	ds_read_b128 v[210:213], v4 offset:0
	ds_read_b128 v[214:217], v2 offset:0x800
	ds_read_b128 v[218:221], v4 offset:0x800
	ds_read_b128 v[222:225], v2 offset:0x1000
	ds_read_b128 v[226:229], v4 offset:0x1000
	ds_read_b128 v[230:233], v2 offset:0x1800
	ds_read_b128 v[234:237], v4 offset:0x1800
	s_waitcnt lgkmcnt(4)
	s_nop 0
	v_mfma_scale_f32_16x16x128_f8f6f4 v[130:133], v[158:165], v[206:213], v[130:133], v178, v178 op_sel_hi:[0,0,0]
	v_mfma_scale_f32_16x16x128_f8f6f4 v[122:125], v[182:189], v[206:213], v[122:125], v178, v178 op_sel_hi:[0,0,0]
	v_mfma_scale_f32_16x16x128_f8f6f4 v[126:129], v[190:197], v[206:213], v[126:129], v178, v178 op_sel_hi:[0,0,0]
	v_mfma_scale_f32_16x16x128_f8f6f4 v[118:121], v[198:205], v[206:213], v[118:121], v178, v178 op_sel_hi:[0,0,0]
	v_mfma_scale_f32_16x16x128_f8f6f4 v[114:117], v[158:165], v[214:221], v[114:117], v178, v178 op_sel_hi:[0,0,0]
	v_mfma_scale_f32_16x16x128_f8f6f4 v[106:109], v[182:189], v[214:221], v[106:109], v178, v178 op_sel_hi:[0,0,0]
	v_mfma_scale_f32_16x16x128_f8f6f4 v[110:113], v[190:197], v[214:221], v[110:113], v178, v178 op_sel_hi:[0,0,0]
	v_mfma_scale_f32_16x16x128_f8f6f4 v[102:105], v[198:205], v[214:221], v[102:105], v178, v178 op_sel_hi:[0,0,0]
	ds_read_b128 v[206:209], v2 offset:0x2000
	ds_read_b128 v[210:213], v4 offset:0x2000
	ds_read_b128 v[214:217], v2 offset:0x2800
	ds_read_b128 v[218:221], v4 offset:0x2800
	s_waitcnt lgkmcnt(4)
	v_mfma_scale_f32_16x16x128_f8f6f4 v[98:101], v[158:165], v[222:229], v[98:101], v178, v178 op_sel_hi:[0,0,0]
	v_mfma_scale_f32_16x16x128_f8f6f4 v[90:93], v[182:189], v[222:229], v[90:93], v178, v178 op_sel_hi:[0,0,0]
	v_mfma_scale_f32_16x16x128_f8f6f4 v[94:97], v[190:197], v[222:229], v[94:97], v178, v178 op_sel_hi:[0,0,0]
	v_mfma_scale_f32_16x16x128_f8f6f4 v[86:89], v[198:205], v[222:229], v[86:89], v178, v178 op_sel_hi:[0,0,0]
	v_mfma_scale_f32_16x16x128_f8f6f4 v[82:85], v[158:165], v[230:237], v[82:85], v178, v178 op_sel_hi:[0,0,0]
	v_mfma_scale_f32_16x16x128_f8f6f4 v[74:77], v[182:189], v[230:237], v[74:77], v178, v178 op_sel_hi:[0,0,0]
	v_mfma_scale_f32_16x16x128_f8f6f4 v[78:81], v[190:197], v[230:237], v[78:81], v178, v178 op_sel_hi:[0,0,0]
	v_mfma_scale_f32_16x16x128_f8f6f4 v[70:73], v[198:205], v[230:237], v[70:73], v178, v178 op_sel_hi:[0,0,0]
	ds_read_b128 v[222:225], v2 offset:0x3000
	ds_read_b128 v[226:229], v4 offset:0x3000
	ds_read_b128 v[230:233], v2 offset:0x3800
	ds_read_b128 v[234:237], v4 offset:0x3800
	s_waitcnt lgkmcnt(0)
	s_branch .LBB0_1032
.LBB0_1051:
	v_writelane_b32 v252, s0, 0
	s_add_i32 s40, s40, 8
	s_cmp_ge_i32 s40, s5
	s_cselect_b64 s[0:1], -1, 0
	s_cmp_lt_i32 s40, s5
	s_cbranch_scc0 .LBB0_1053
	s_waitcnt vmcnt(0)
.LBB0_1053:
	s_waitcnt lgkmcnt(0)
	s_barrier
	v_readlane_b32 vcc_lo, v252, 0
	s_nop 3
	s_cmp_eq_u32 vcc_lo, 0
	s_cbranch_scc1 .Lp5a_notail
	s_cmp_lt_u32 s4, 0x4000
	s_cbranch_scc1 .Lp5a_notail
	v_mfma_scale_f32_16x16x128_f8f6f4 v[66:69], v[158:165], v[206:213], v[66:69], v178, v178 op_sel_hi:[0,0,0]
	v_mfma_scale_f32_16x16x128_f8f6f4 v[58:61], v[182:189], v[206:213], v[58:61], v178, v178 op_sel_hi:[0,0,0]
	v_mfma_scale_f32_16x16x128_f8f6f4 v[62:65], v[190:197], v[206:213], v[62:65], v178, v178 op_sel_hi:[0,0,0]
	v_mfma_scale_f32_16x16x128_f8f6f4 v[54:57], v[198:205], v[206:213], v[54:57], v178, v178 op_sel_hi:[0,0,0]
	v_mfma_scale_f32_16x16x128_f8f6f4 v[50:53], v[158:165], v[214:221], v[50:53], v178, v178 op_sel_hi:[0,0,0]
	v_mfma_scale_f32_16x16x128_f8f6f4 v[42:45], v[182:189], v[214:221], v[42:45], v178, v178 op_sel_hi:[0,0,0]
	v_mfma_scale_f32_16x16x128_f8f6f4 v[46:49], v[190:197], v[214:221], v[46:49], v178, v178 op_sel_hi:[0,0,0]
	v_mfma_scale_f32_16x16x128_f8f6f4 v[38:41], v[198:205], v[214:221], v[38:41], v178, v178 op_sel_hi:[0,0,0]
	v_mfma_scale_f32_16x16x128_f8f6f4 v[34:37], v[158:165], v[222:229], v[34:37], v178, v178 op_sel_hi:[0,0,0]
	v_mfma_scale_f32_16x16x128_f8f6f4 v[26:29], v[182:189], v[222:229], v[26:29], v178, v178 op_sel_hi:[0,0,0]
	v_mfma_scale_f32_16x16x128_f8f6f4 v[30:33], v[190:197], v[222:229], v[30:33], v178, v178 op_sel_hi:[0,0,0]
	v_mfma_scale_f32_16x16x128_f8f6f4 v[22:25], v[198:205], v[222:229], v[22:25], v178, v178 op_sel_hi:[0,0,0]
	v_mfma_scale_f32_16x16x128_f8f6f4 v[18:21], v[158:165], v[230:237], v[18:21], v178, v178 op_sel_hi:[0,0,0]
	v_mfma_scale_f32_16x16x128_f8f6f4 v[10:13], v[182:189], v[230:237], v[10:13], v178, v178 op_sel_hi:[0,0,0]
	v_mfma_scale_f32_16x16x128_f8f6f4 v[14:17], v[190:197], v[230:237], v[14:17], v178, v178 op_sel_hi:[0,0,0]
	v_mfma_scale_f32_16x16x128_f8f6f4 v[6:9], v[198:205], v[230:237], v[6:9], v178, v178 op_sel_hi:[0,0,0]
	s_nop 7
	s_nop 4
.Lp5a_notail:
	v_mov_b32_e32 v183, v0
	v_mov_b32_e32 v182, v0
	v_mov_b32_e32 v2, v0
	v_mov_b64_e32 v[158:159], -1
	v_ashrrev_i32_e32 v160, 3, v2
	v_cmp_lt_i32_e32 vcc, v160, v180
	v_ashrrev_i32_e32 v161, 31, v160
	v_mov_b64_e32 v[162:163], -1
	s_and_saveexec_b64 s[16:17], vcc
	s_cbranch_execz .LBB0_1055
	v_lshl_add_u64 v[4:5], v[160:161], 2, v[156:157]
	global_load_dword v162, v[4:5], off
; __device__ __forceinline__ int pack4_fp8(float a, float b, float c, float d) { int w = __builtin_amdgcn_cvt_pk_fp8_f32(a, b, 0, false); return __builtin_amdgcn_cvt_pk_fp8_f32(c, d, w, true); }
; __device__ __forceinline__ int otid() { int t = threadIdx.x; asm volatile("" : "+v"(t)); return t; }
; template <class SlotF>
; __device__ __forceinline__ void swiglu_store8(const f32x4 (&acc)[8][4], int jt, unsigned char* act8, SlotF slotf, unsigned char* tile, float sc, bool wact) {
;     ...
;     long sl0 = slotf((tid >> 3)), sl1 = slotf((tid >> 3) + 64), sl2 = slotf((tid >> 3) + 128), sl3 = slotf((tid >> 3) + 192);
;     if (wact) {
;         const float k1 = -sc * L2E, k2 = sc * sc * A8S;
; #pragma unroll
;         for (int m = 0; m < 8; ++m) {
;             const int row = wr * 128 + m * 16 + l15;
; #pragma unroll
;             for (int n = 0; n < 2; ++n) {
;                 f32x4 v;
; #pragma unroll
;                 for (int r = 0; r < 4; ++r) {
;                     const float ag = acc[m][n][r], au = acc[m][n + 2][r];
;                     const float rr = __builtin_amdgcn_rcpf(1.f + __builtin_amdgcn_exp2f(ag * k1));
;                     v[r] = __builtin_amdgcn_fmed3f((ag * au) * (rr * k2), -440.f, 440.f);
;                 }
;                 *(int*)(tile + row * 128 + (((wc * 2 + n) ^ (row & 7)) << 4) + gq * 4) = pack4_fp8(v[0], v[1], v[2], v[3]);
;     __device__ __forceinline__ void epilogue(f32x4 (&acc)[8][4], const Desc& d, unsigned char* stg) const {
;     ...
;         swiglu_store8(acc, d.jt, (unsigned char*)p.act, [&](int rowl) -> long { return rowl < nrow ? (long)lst[rowl] : -1L; }, stg - (otid() >> 6) * STG_WAVE, 1.f / (W8S * H8S), (otid() >> 8) * 128 < nrow);
.LBB0_1055:
	s_or_b64 exec, exec, s[16:17]
	v_add_u32_e32 v4, 64, v160
	v_cmp_lt_i32_e32 vcc, v4, v180
	s_and_saveexec_b64 s[16:17], vcc
	s_cbranch_execz .LBB0_1057
	v_lshl_add_u64 v[158:159], v[160:161], 2, v[156:157]
	global_load_dword v158, v[158:159], off offset:256
.LBB0_1057:
	s_or_b64 exec, exec, s[16:17]
	v_add_u32_e32 v5, 0x80, v160
	v_cmp_lt_i32_e32 vcc, v5, v180
	v_mov_b64_e32 v[164:165], -1
	v_mov_b64_e32 v[166:167], -1
	s_and_saveexec_b64 s[16:17], vcc
	s_cbranch_execz .LBB0_1059
	v_lshl_add_u64 v[166:167], v[160:161], 2, v[156:157]
	global_load_dword v166, v[166:167], off offset:512
.LBB0_1059:
	s_or_b64 exec, exec, s[16:17]
	v_add_u32_e32 v181, 0xc0, v160
	v_cmp_lt_i32_e32 vcc, v181, v180
	s_and_saveexec_b64 s[16:17], vcc
	s_cbranch_execz .LBB0_1061
	v_lshl_add_u64 v[156:157], v[160:161], 2, v[156:157]
	global_load_dword v164, v[156:157], off offset:768
.LBB0_1061:
	s_or_b64 exec, exec, s[16:17]
	v_lshlrev_b32_e32 v156, 6, v183
	v_ashrrev_i32_e32 v157, 1, v182
	v_and_b32_e32 v156, 0xfffff000, v156
	v_and_b32_e32 v157, 0xffffff80, v157
	v_sub_u32_e32 v156, s20, v156
	v_cmp_lt_i32_e32 vcc, v157, v180
	s_and_saveexec_b64 s[16:17], vcc
	s_cbranch_execz .LBB0_1063
	v_mul_f32_e32 v184, 0xbab8aa3b, v130
	v_exp_f32_e32 v184, v184
	v_and_b32_e32 v157, 15, v2
	v_lshrrev_b32_e32 v161, 1, v2
	v_and_or_b32 v157, v161, s22, v157
	v_lshrrev_b32_e32 v183, 2, v2
	v_and_b32_e32 v183, 12, v183
	v_lshlrev_b32_e32 v157, 7, v157
	v_add3_u32 v157, v156, v183, v157
	v_add_f32_e32 v183, 1.0, v184
	v_mul_f32_e32 v126, v126, v130
	v_mul_f32_e32 v130, 0xbab8aa3b, v131
	v_rcp_f32_e32 v183, v183
	v_exp_f32_e32 v130, v130
	v_mul_f32_e32 v127, v127, v131
	v_mul_f32_e32 v131, 0xbab8aa3b, v133
	v_mul_f32_e32 v183, 0x36800000, v183
	v_add_f32_e32 v130, 1.0, v130
	v_mul_f32_e32 v126, v126, v183
	v_rcp_f32_e32 v130, v130
	v_mul_f32_e32 v183, 0xbab8aa3b, v132
	v_exp_f32_e32 v183, v183
	v_exp_f32_e32 v131, v131
	v_mul_f32_e32 v130, 0x36800000, v130
	v_mul_f32_e32 v127, v127, v130
	v_add_f32_e32 v130, 1.0, v183
	v_rcp_f32_e32 v130, v130
	v_add_f32_e32 v131, 1.0, v131
	v_rcp_f32_e32 v131, v131
	v_mul_f32_e32 v128, v128, v132
	v_mul_f32_e32 v130, 0x36800000, v130
	v_mul_f32_e32 v128, v128, v130
	v_mul_f32_e32 v129, v129, v133
	v_mul_f32_e32 v130, 0x36800000, v131
	v_med3_f32 v126, v126, s23, v179
	v_med3_f32 v127, v127, s23, v179
	v_mul_f32_e32 v129, v129, v130
	v_mov_b32_e32 v130, v3
	v_cvt_pk_fp8_f32 v130, v126, v127
	v_mul_f32_e32 v127, 0xbab8aa3b, v122
	v_exp_f32_e32 v127, v127
	v_mul_f32_e32 v118, v118, v122
	v_mul_f32_e32 v122, 0xbab8aa3b, v123
	v_exp_f32_e32 v122, v122
	v_add_f32_e32 v127, 1.0, v127
	v_rcp_f32_e32 v127, v127
	v_mul_f32_e32 v119, v119, v123
	v_add_f32_e32 v122, 1.0, v122
	v_rcp_f32_e32 v122, v122
	v_mul_f32_e32 v127, 0x36800000, v127
	v_mul_f32_e32 v118, v118, v127
	v_mul_f32_e32 v127, 0xbab8aa3b, v124
	v_exp_f32_e32 v127, v127
	v_mul_f32_e32 v123, 0xbab8aa3b, v125
	v_exp_f32_e32 v123, v123
	v_mul_f32_e32 v122, 0x36800000, v122
	v_mul_f32_e32 v119, v119, v122
	v_add_f32_e32 v122, 1.0, v127
	v_rcp_f32_e32 v122, v122
	v_add_f32_e32 v123, 1.0, v123
	v_rcp_f32_e32 v123, v123
	v_mul_f32_e32 v120, v120, v124
	v_mul_f32_e32 v122, 0x36800000, v122
	v_med3_f32 v118, v118, s23, v179
	v_med3_f32 v119, v119, s23, v179
	v_mul_f32_e32 v120, v120, v122
	v_mul_f32_e32 v122, 0x36800000, v123
	v_mov_b32_e32 v123, v3
	v_cvt_pk_fp8_f32 v123, v118, v119
	v_mul_f32_e32 v118, 0xbab8aa3b, v114
	v_mul_f32_e32 v110, v110, v114
	v_mul_f32_e32 v114, 0xbab8aa3b, v115
	v_exp_f32_e32 v114, v114
	v_mul_f32_e32 v111, v111, v115
	v_mul_f32_e32 v115, 0xbab8aa3b, v116
	v_exp_f32_e32 v115, v115
	v_add_f32_e32 v114, 1.0, v114
	v_rcp_f32_e32 v114, v114
	v_exp_f32_e32 v118, v118
	v_mul_f32_e32 v112, v112, v116
	v_mul_f32_e32 v113, v113, v117
	v_mul_f32_e32 v114, 0x36800000, v114
	v_mul_f32_e32 v111, v111, v114
	v_add_f32_e32 v114, 1.0, v115
	v_rcp_f32_e32 v114, v114
	v_mul_f32_e32 v115, 0xbab8aa3b, v117
	v_add_f32_e32 v118, 1.0, v118
	v_exp_f32_e32 v115, v115
	v_rcp_f32_e32 v118, v118
	v_mul_f32_e32 v114, 0x36800000, v114
	v_mul_f32_e32 v112, v112, v114
	v_add_f32_e32 v114, 1.0, v115
	v_mul_f32_e32 v118, 0x36800000, v118
	v_rcp_f32_e32 v114, v114
	v_mul_f32_e32 v110, v110, v118
	v_med3_f32 v110, v110, s23, v179
	v_med3_f32 v111, v111, s23, v179
	v_mov_b32_e32 v115, v3
	v_cvt_pk_fp8_f32 v115, v110, v111
	v_mul_f32_e32 v110, 0x36800000, v114
	v_mul_f32_e32 v110, v113, v110
	v_med3_f32 v112, v112, s23, v179
	v_med3_f32 v110, v110, s23, v179
	v_cvt_pk_fp8_f32 v115, v112, v110 op_sel:[0,0,1]
	v_mul_f32_e32 v110, 0xbab8aa3b, v106
	v_exp_f32_e32 v111, v110
	v_mul_f32_e32 v102, v102, v106
	v_mul_f32_e32 v106, 0xbab8aa3b, v107
	v_exp_f32_e32 v106, v106
	v_add_f32_e32 v111, 1.0, v111
	v_rcp_f32_e32 v111, v111
	v_mul_f32_e32 v103, v103, v107
	v_add_f32_e32 v106, 1.0, v106
	v_rcp_f32_e32 v106, v106
	v_mul_f32_e32 v111, 0x36800000, v111
	v_mul_f32_e32 v102, v102, v111
	v_mul_f32_e32 v111, 0xbab8aa3b, v108
	v_exp_f32_e32 v111, v111
	v_mul_f32_e32 v107, 0xbab8aa3b, v109
	v_exp_f32_e32 v107, v107
	v_mul_f32_e32 v106, 0x36800000, v106
	v_mul_f32_e32 v103, v103, v106
	v_add_f32_e32 v106, 1.0, v111
	v_rcp_f32_e32 v106, v106
	v_add_f32_e32 v107, 1.0, v107
	v_rcp_f32_e32 v107, v107
	v_mul_f32_e32 v104, v104, v108
	v_mul_f32_e32 v106, 0x36800000, v106
	v_med3_f32 v102, v102, s23, v179
	v_med3_f32 v103, v103, s23, v179
	v_mul_f32_e32 v104, v104, v106
	v_mul_f32_e32 v106, 0x36800000, v107
	v_mov_b32_e32 v107, v3
	v_cvt_pk_fp8_f32 v107, v102, v103
	v_mul_f32_e32 v102, 0xbab8aa3b, v98
	v_exp_f32_e32 v102, v102
	v_mul_f32_e32 v94, v94, v98
	v_mul_f32_e32 v98, 0xbab8aa3b, v99
	v_exp_f32_e32 v98, v98
; __device__ __forceinline__ int pack4_fp8(float a, float b, float c, float d) { int w = __builtin_amdgcn_cvt_pk_fp8_f32(a, b, 0, false); return __builtin_amdgcn_cvt_pk_fp8_f32(c, d, w, true); }
; template <class SlotF>
; __device__ __forceinline__ void swiglu_store8(const f32x4 (&acc)[8][4], int jt, unsigned char* act8, SlotF slotf, unsigned char* tile, float sc, bool wact) {
;     ...
;         for (int m = 0; m < 8; ++m) {
;             const int row = wr * 128 + m * 16 + l15;
; #pragma unroll
;             for (int n = 0; n < 2; ++n) {
;                 f32x4 v;
; #pragma unroll
;                 for (int r = 0; r < 4; ++r) {
;                     const float ag = acc[m][n][r], au = acc[m][n + 2][r];
;                     const float rr = __builtin_amdgcn_rcpf(1.f + __builtin_amdgcn_exp2f(ag * k1));
;                     v[r] = __builtin_amdgcn_fmed3f((ag * au) * (rr * k2), -440.f, 440.f);
;                 }
;                 *(int*)(tile + row * 128 + (((wc * 2 + n) ^ (row & 7)) << 4) + gq * 4) = pack4_fp8(v[0], v[1], v[2], v[3]);
	v_add_f32_e32 v102, 1.0, v102
	v_rcp_f32_e32 v102, v102
	v_mul_f32_e32 v95, v95, v99
	v_add_f32_e32 v98, 1.0, v98
	v_rcp_f32_e32 v98, v98
	v_mul_f32_e32 v102, 0x36800000, v102
	v_mul_f32_e32 v94, v94, v102
	v_mul_f32_e32 v102, 0xbab8aa3b, v100
	v_exp_f32_e32 v102, v102
	v_mul_f32_e32 v99, 0xbab8aa3b, v101
	v_exp_f32_e32 v99, v99
	v_mul_f32_e32 v98, 0x36800000, v98
	v_mul_f32_e32 v95, v95, v98
	v_add_f32_e32 v98, 1.0, v102
	v_rcp_f32_e32 v98, v98
	v_add_f32_e32 v99, 1.0, v99
	v_rcp_f32_e32 v99, v99
	v_mul_f32_e32 v96, v96, v100
	v_mul_f32_e32 v98, 0x36800000, v98
	v_med3_f32 v94, v94, s23, v179
	v_med3_f32 v95, v95, s23, v179
	v_mul_f32_e32 v96, v96, v98
	v_mul_f32_e32 v98, 0x36800000, v99
	v_mov_b32_e32 v99, v3
	v_cvt_pk_fp8_f32 v99, v94, v95
	v_mul_f32_e32 v94, 0xbab8aa3b, v90
	v_exp_f32_e32 v94, v94
	v_mul_f32_e32 v86, v86, v90
	v_mul_f32_e32 v90, 0xbab8aa3b, v91
	v_exp_f32_e32 v90, v90
	v_add_f32_e32 v94, 1.0, v94
	v_rcp_f32_e32 v94, v94
	v_mul_f32_e32 v87, v87, v91
	v_add_f32_e32 v90, 1.0, v90
	v_rcp_f32_e32 v90, v90
	v_mul_f32_e32 v94, 0x36800000, v94
	v_mul_f32_e32 v86, v86, v94
	v_mul_f32_e32 v94, 0xbab8aa3b, v92
	v_exp_f32_e32 v94, v94
	v_mul_f32_e32 v91, 0xbab8aa3b, v93
	v_exp_f32_e32 v91, v91
	v_mul_f32_e32 v90, 0x36800000, v90
	v_mul_f32_e32 v87, v87, v90
	v_add_f32_e32 v90, 1.0, v94
	v_rcp_f32_e32 v90, v90
	v_add_f32_e32 v91, 1.0, v91
	v_rcp_f32_e32 v91, v91
	v_mul_f32_e32 v88, v88, v92
	v_mul_f32_e32 v90, 0x36800000, v90
	v_med3_f32 v86, v86, s23, v179
	v_med3_f32 v87, v87, s23, v179
	v_mul_f32_e32 v88, v88, v90
	v_mul_f32_e32 v90, 0x36800000, v91
	v_mov_b32_e32 v91, v3
	v_cvt_pk_fp8_f32 v91, v86, v87
	v_mul_f32_e32 v86, 0xbab8aa3b, v82
	v_exp_f32_e32 v86, v86
	v_mul_f32_e32 v78, v78, v82
	v_mul_f32_e32 v82, 0xbab8aa3b, v83
	v_exp_f32_e32 v82, v82
	v_add_f32_e32 v86, 1.0, v86
	v_rcp_f32_e32 v86, v86
	v_mul_f32_e32 v79, v79, v83
	v_add_f32_e32 v82, 1.0, v82
	v_rcp_f32_e32 v82, v82
	v_mul_f32_e32 v86, 0x36800000, v86
	v_mul_f32_e32 v78, v78, v86
	v_mul_f32_e32 v86, 0xbab8aa3b, v84
	v_exp_f32_e32 v86, v86
	v_mul_f32_e32 v83, 0xbab8aa3b, v85
	v_exp_f32_e32 v83, v83
	v_mul_f32_e32 v82, 0x36800000, v82
	v_mul_f32_e32 v79, v79, v82
	v_add_f32_e32 v82, 1.0, v86
	v_rcp_f32_e32 v82, v82
	v_add_f32_e32 v83, 1.0, v83
	v_rcp_f32_e32 v83, v83
	v_mul_f32_e32 v80, v80, v84
	v_mul_f32_e32 v82, 0x36800000, v82
	v_med3_f32 v78, v78, s23, v179
	v_med3_f32 v79, v79, s23, v179
	v_mul_f32_e32 v80, v80, v82
	v_mul_f32_e32 v82, 0x36800000, v83
	v_mov_b32_e32 v83, v3
	v_cvt_pk_fp8_f32 v83, v78, v79
	v_mul_f32_e32 v78, 0xbab8aa3b, v74
	v_mul_f32_e32 v70, v70, v74
	v_mul_f32_e32 v74, 0xbab8aa3b, v75
	v_exp_f32_e32 v74, v74
	v_mul_f32_e32 v71, v71, v75
	v_mul_f32_e32 v75, 0xbab8aa3b, v76
	v_exp_f32_e32 v75, v75
	v_add_f32_e32 v74, 1.0, v74
	v_rcp_f32_e32 v74, v74
	v_exp_f32_e32 v78, v78
	v_mul_f32_e32 v72, v72, v76
	v_mul_f32_e32 v73, v73, v77
	v_mul_f32_e32 v74, 0x36800000, v74
	v_mul_f32_e32 v71, v71, v74
	v_add_f32_e32 v74, 1.0, v75
	v_rcp_f32_e32 v74, v74
	v_mul_f32_e32 v75, 0xbab8aa3b, v77
	v_add_f32_e32 v78, 1.0, v78
	v_exp_f32_e32 v75, v75
	v_rcp_f32_e32 v78, v78
	v_mul_f32_e32 v74, 0x36800000, v74
	v_mul_f32_e32 v72, v72, v74
	v_add_f32_e32 v74, 1.0, v75
	v_mul_f32_e32 v78, 0x36800000, v78
	v_rcp_f32_e32 v74, v74
	v_mul_f32_e32 v70, v70, v78
	v_med3_f32 v70, v70, s23, v179
	v_med3_f32 v71, v71, s23, v179
	v_mov_b32_e32 v75, v3
	v_cvt_pk_fp8_f32 v75, v70, v71
	v_mul_f32_e32 v70, 0x36800000, v74
	v_mul_f32_e32 v70, v73, v70
	v_med3_f32 v72, v72, s23, v179
	v_med3_f32 v70, v70, s23, v179
	v_cvt_pk_fp8_f32 v75, v72, v70 op_sel:[0,0,1]
	v_mul_f32_e32 v70, 0xbab8aa3b, v66
	v_exp_f32_e32 v70, v70
	v_mul_f32_e32 v62, v62, v66
	v_mul_f32_e32 v66, 0xbab8aa3b, v67
	v_exp_f32_e32 v66, v66
	v_add_f32_e32 v70, 1.0, v70
	v_rcp_f32_e32 v70, v70
	v_mul_f32_e32 v63, v63, v67
	v_add_f32_e32 v66, 1.0, v66
	v_rcp_f32_e32 v66, v66
	v_mul_f32_e32 v70, 0x36800000, v70
	v_mul_f32_e32 v62, v62, v70
	v_mul_f32_e32 v70, 0xbab8aa3b, v68
	v_exp_f32_e32 v70, v70
	v_mul_f32_e32 v67, 0xbab8aa3b, v69
	v_exp_f32_e32 v67, v67
	v_mul_f32_e32 v66, 0x36800000, v66
	v_mul_f32_e32 v63, v63, v66
	v_add_f32_e32 v66, 1.0, v70
	v_rcp_f32_e32 v66, v66
	v_add_f32_e32 v67, 1.0, v67
	v_rcp_f32_e32 v67, v67
	v_mul_f32_e32 v64, v64, v68
	v_mul_f32_e32 v66, 0x36800000, v66
	v_med3_f32 v62, v62, s23, v179
	v_med3_f32 v63, v63, s23, v179
	v_mul_f32_e32 v64, v64, v66
	v_mul_f32_e32 v66, 0x36800000, v67
	v_mov_b32_e32 v67, v3
	v_cvt_pk_fp8_f32 v67, v62, v63
	v_mul_f32_e32 v62, 0xbab8aa3b, v58
	v_exp_f32_e32 v62, v62
	v_mul_f32_e32 v54, v54, v58
	v_mul_f32_e32 v58, 0xbab8aa3b, v59
	v_exp_f32_e32 v58, v58
	v_add_f32_e32 v62, 1.0, v62
	v_rcp_f32_e32 v62, v62
	v_mul_f32_e32 v55, v55, v59
	v_add_f32_e32 v58, 1.0, v58
	v_rcp_f32_e32 v58, v58
	v_mul_f32_e32 v62, 0x36800000, v62
	v_mul_f32_e32 v54, v54, v62
	v_mul_f32_e32 v62, 0xbab8aa3b, v60
	v_exp_f32_e32 v62, v62
	v_mul_f32_e32 v59, 0xbab8aa3b, v61
	v_exp_f32_e32 v59, v59
	v_mul_f32_e32 v58, 0x36800000, v58
	v_mul_f32_e32 v55, v55, v58
	v_add_f32_e32 v58, 1.0, v62
	v_rcp_f32_e32 v58, v58
	v_add_f32_e32 v59, 1.0, v59
	v_rcp_f32_e32 v59, v59
	v_mul_f32_e32 v56, v56, v60
	v_mul_f32_e32 v58, 0x36800000, v58
	v_med3_f32 v54, v54, s23, v179
	v_med3_f32 v55, v55, s23, v179
	v_mul_f32_e32 v56, v56, v58
	v_mul_f32_e32 v58, 0x36800000, v59
	v_mov_b32_e32 v59, v3
	v_cvt_pk_fp8_f32 v59, v54, v55
	v_mul_f32_e32 v54, 0xbab8aa3b, v50
	v_exp_f32_e32 v54, v54
	v_mul_f32_e32 v46, v46, v50
	v_mul_f32_e32 v50, 0xbab8aa3b, v51
	v_exp_f32_e32 v50, v50
	v_add_f32_e32 v54, 1.0, v54
	v_rcp_f32_e32 v54, v54
	v_mul_f32_e32 v47, v47, v51
	v_add_f32_e32 v50, 1.0, v50
; __device__ __forceinline__ int pack4_fp8(float a, float b, float c, float d) { int w = __builtin_amdgcn_cvt_pk_fp8_f32(a, b, 0, false); return __builtin_amdgcn_cvt_pk_fp8_f32(c, d, w, true); }
; template <class SlotF>
; __device__ __forceinline__ void swiglu_store8(const f32x4 (&acc)[8][4], int jt, unsigned char* act8, SlotF slotf, unsigned char* tile, float sc, bool wact) {
;     ...
;         for (int m = 0; m < 8; ++m) {
;             const int row = wr * 128 + m * 16 + l15;
; #pragma unroll
;             for (int n = 0; n < 2; ++n) {
;                 f32x4 v;
; #pragma unroll
;                 for (int r = 0; r < 4; ++r) {
;                     const float ag = acc[m][n][r], au = acc[m][n + 2][r];
;                     const float rr = __builtin_amdgcn_rcpf(1.f + __builtin_amdgcn_exp2f(ag * k1));
;                     v[r] = __builtin_amdgcn_fmed3f((ag * au) * (rr * k2), -440.f, 440.f);
;                 }
;                 *(int*)(tile + row * 128 + (((wc * 2 + n) ^ (row & 7)) << 4) + gq * 4) = pack4_fp8(v[0], v[1], v[2], v[3]);
	v_rcp_f32_e32 v50, v50
	v_mul_f32_e32 v54, 0x36800000, v54
	v_mul_f32_e32 v46, v46, v54
	v_mul_f32_e32 v54, 0xbab8aa3b, v52
	v_exp_f32_e32 v54, v54
	v_mul_f32_e32 v51, 0xbab8aa3b, v53
	v_exp_f32_e32 v51, v51
	v_mul_f32_e32 v50, 0x36800000, v50
	v_mul_f32_e32 v47, v47, v50
	v_add_f32_e32 v50, 1.0, v54
	v_rcp_f32_e32 v50, v50
	v_add_f32_e32 v51, 1.0, v51
	v_rcp_f32_e32 v51, v51
	v_mul_f32_e32 v48, v48, v52
	v_mul_f32_e32 v50, 0x36800000, v50
	v_med3_f32 v46, v46, s23, v179
	v_med3_f32 v47, v47, s23, v179
	v_mul_f32_e32 v48, v48, v50
	v_mul_f32_e32 v50, 0x36800000, v51
	v_mov_b32_e32 v51, v3
	v_cvt_pk_fp8_f32 v51, v46, v47
	v_mul_f32_e32 v46, 0xbab8aa3b, v42
	v_exp_f32_e32 v46, v46
	v_mul_f32_e32 v38, v38, v42
	v_mul_f32_e32 v42, 0xbab8aa3b, v43
	v_exp_f32_e32 v42, v42
	v_add_f32_e32 v46, 1.0, v46
	v_rcp_f32_e32 v46, v46
	v_mul_f32_e32 v39, v39, v43
	v_add_f32_e32 v42, 1.0, v42
	v_rcp_f32_e32 v42, v42
	v_mul_f32_e32 v46, 0x36800000, v46
	v_mul_f32_e32 v38, v38, v46
	v_mul_f32_e32 v46, 0xbab8aa3b, v44
	v_exp_f32_e32 v46, v46
	v_mul_f32_e32 v43, 0xbab8aa3b, v45
	v_exp_f32_e32 v43, v43
	v_mul_f32_e32 v42, 0x36800000, v42
	v_mul_f32_e32 v39, v39, v42
	v_add_f32_e32 v42, 1.0, v46
	v_rcp_f32_e32 v42, v42
	v_add_f32_e32 v43, 1.0, v43
	v_rcp_f32_e32 v43, v43
	v_mul_f32_e32 v40, v40, v44
	v_mul_f32_e32 v42, 0x36800000, v42
	v_med3_f32 v38, v38, s23, v179
	v_med3_f32 v39, v39, s23, v179
	v_mul_f32_e32 v40, v40, v42
	v_mul_f32_e32 v42, 0x36800000, v43
	v_mov_b32_e32 v43, v3
	v_cvt_pk_fp8_f32 v43, v38, v39
	v_mul_f32_e32 v38, 0xbab8aa3b, v34
	v_exp_f32_e32 v38, v38
	v_mul_f32_e32 v30, v30, v34
	v_mul_f32_e32 v34, 0xbab8aa3b, v35
	v_exp_f32_e32 v34, v34
	v_add_f32_e32 v38, 1.0, v38
	v_rcp_f32_e32 v38, v38
	v_mul_f32_e32 v31, v31, v35
	v_add_f32_e32 v34, 1.0, v34
	v_rcp_f32_e32 v34, v34
	v_mul_f32_e32 v38, 0x36800000, v38
	v_mul_f32_e32 v30, v30, v38
	v_mul_f32_e32 v38, 0xbab8aa3b, v36
	v_exp_f32_e32 v38, v38
	v_mul_f32_e32 v35, 0xbab8aa3b, v37
	v_exp_f32_e32 v35, v35
	v_mul_f32_e32 v34, 0x36800000, v34
	v_mul_f32_e32 v31, v31, v34
	v_add_f32_e32 v34, 1.0, v38
	v_rcp_f32_e32 v34, v34
	v_add_f32_e32 v35, 1.0, v35
	v_rcp_f32_e32 v35, v35
	v_mul_f32_e32 v32, v32, v36
	v_mul_f32_e32 v34, 0x36800000, v34
	v_med3_f32 v30, v30, s23, v179
	v_med3_f32 v31, v31, s23, v179
	v_mul_f32_e32 v32, v32, v34
	v_mul_f32_e32 v34, 0x36800000, v35
	v_mov_b32_e32 v35, v3
	v_cvt_pk_fp8_f32 v35, v30, v31
	v_mul_f32_e32 v30, 0xbab8aa3b, v26
	v_exp_f32_e32 v30, v30
	v_mul_f32_e32 v22, v22, v26
	v_mul_f32_e32 v26, 0xbab8aa3b, v27
	v_exp_f32_e32 v26, v26
	v_add_f32_e32 v30, 1.0, v30
	v_rcp_f32_e32 v30, v30
	v_mul_f32_e32 v23, v23, v27
	v_add_f32_e32 v26, 1.0, v26
	v_rcp_f32_e32 v26, v26
	v_mul_f32_e32 v30, 0x36800000, v30
	v_mul_f32_e32 v22, v22, v30
	v_mul_f32_e32 v30, 0xbab8aa3b, v28
	v_exp_f32_e32 v30, v30
	v_mul_f32_e32 v27, 0xbab8aa3b, v29
	v_exp_f32_e32 v27, v27
	v_mul_f32_e32 v26, 0x36800000, v26
	v_mul_f32_e32 v23, v23, v26
	v_add_f32_e32 v26, 1.0, v30
	v_rcp_f32_e32 v26, v26
	v_add_f32_e32 v27, 1.0, v27
	v_rcp_f32_e32 v27, v27
	v_mul_f32_e32 v24, v24, v28
	v_mul_f32_e32 v26, 0x36800000, v26
	v_med3_f32 v22, v22, s23, v179
	v_med3_f32 v23, v23, s23, v179
	v_mul_f32_e32 v24, v24, v26
	v_mul_f32_e32 v26, 0x36800000, v27
	v_mov_b32_e32 v27, v3
	v_cvt_pk_fp8_f32 v27, v22, v23
	v_mul_f32_e32 v22, 0xbab8aa3b, v18
	v_exp_f32_e32 v22, v22
	v_mul_f32_e32 v14, v14, v18
	v_mul_f32_e32 v18, 0xbab8aa3b, v19
	v_exp_f32_e32 v18, v18
	v_add_f32_e32 v22, 1.0, v22
	v_rcp_f32_e32 v22, v22
	v_mul_f32_e32 v15, v15, v19
	v_add_f32_e32 v18, 1.0, v18
	v_rcp_f32_e32 v18, v18
	v_mul_f32_e32 v22, 0x36800000, v22
	v_mul_f32_e32 v14, v14, v22
	v_mul_f32_e32 v22, 0xbab8aa3b, v20
	v_exp_f32_e32 v22, v22
	v_mul_f32_e32 v19, 0xbab8aa3b, v21
	v_exp_f32_e32 v19, v19
	v_mul_f32_e32 v18, 0x36800000, v18
	v_mul_f32_e32 v15, v15, v18
	v_add_f32_e32 v18, 1.0, v22
	v_rcp_f32_e32 v18, v18
	v_add_f32_e32 v19, 1.0, v19
	v_rcp_f32_e32 v19, v19
	v_mul_f32_e32 v16, v16, v20
	v_mul_f32_e32 v18, 0x36800000, v18
	v_med3_f32 v14, v14, s23, v179
	v_med3_f32 v15, v15, s23, v179
	v_mul_f32_e32 v16, v16, v18
	v_mul_f32_e32 v18, 0x36800000, v19
	v_mov_b32_e32 v19, v3
	v_cvt_pk_fp8_f32 v19, v14, v15
	v_mul_f32_e32 v14, 0xbab8aa3b, v10
	v_mul_f32_e32 v6, v6, v10
	v_mul_f32_e32 v10, 0xbab8aa3b, v11
	v_exp_f32_e32 v10, v10
	v_mul_f32_e32 v7, v7, v11
	v_mul_f32_e32 v11, 0xbab8aa3b, v12
	v_exp_f32_e32 v11, v11
	v_add_f32_e32 v10, 1.0, v10
	v_rcp_f32_e32 v10, v10
	v_exp_f32_e32 v14, v14
	v_mul_f32_e32 v8, v8, v12
	v_mul_f32_e32 v121, v121, v125
; __device__ __forceinline__ int pack4_fp8(float a, float b, float c, float d) { int w = __builtin_amdgcn_cvt_pk_fp8_f32(a, b, 0, false); return __builtin_amdgcn_cvt_pk_fp8_f32(c, d, w, true); }
; template <class SlotF>
; __device__ __forceinline__ void swiglu_store8(const f32x4 (&acc)[8][4], int jt, unsigned char* act8, SlotF slotf, unsigned char* tile, float sc, bool wact) {
;     ...
;         for (int m = 0; m < 8; ++m) {
;             const int row = wr * 128 + m * 16 + l15;
; #pragma unroll
;             for (int n = 0; n < 2; ++n) {
;                 f32x4 v;
; #pragma unroll
;                 for (int r = 0; r < 4; ++r) {
;                     const float ag = acc[m][n][r], au = acc[m][n + 2][r];
;                     const float rr = __builtin_amdgcn_rcpf(1.f + __builtin_amdgcn_exp2f(ag * k1));
;                     v[r] = __builtin_amdgcn_fmed3f((ag * au) * (rr * k2), -440.f, 440.f);
;                 }
;                 *(int*)(tile + row * 128 + (((wc * 2 + n) ^ (row & 7)) << 4) + gq * 4) = pack4_fp8(v[0], v[1], v[2], v[3]);
;             }
;         }
;     }
;     asm volatile("s_waitcnt lgkmcnt(0)" ::: "memory"); __builtin_amdgcn_s_barrier(); asm volatile("" ::: "memory");
;     unsigned char* abase = act8 + jt * 128 + (tid & 7) * 16;
;     {
;         const int r0 = tid >> 3, ch = tid & 7;
;         const uint4 w0 = *(const uint4*)(tile + r0 * 128 + ((ch ^ (r0 & 7)) << 4)), w1 = *(const uint4*)(tile + (r0 + 64) * 128 + ((ch ^ (r0 & 7)) << 4));
;         const uint4 w2 = *(const uint4*)(tile + (r0 + 128) * 128 + ((ch ^ (r0 & 7)) << 4)), w3 = *(const uint4*)(tile + (r0 + 192) * 128 + ((ch ^ (r0 & 7)) << 4));
;         if (sl0 >= 0) *(uint4*)(abase + (size_t)sl0 * 256) = w0;
;         if (sl1 >= 0) *(uint4*)(abase + (size_t)sl1 * 256) = w1;
;         if (sl2 >= 0) *(uint4*)(abase + (size_t)sl2 * 256) = w2;
;         if (sl3 >= 0) *(uint4*)(abase + (size_t)sl3 * 256) = w3;
	v_mul_f32_e32 v10, 0x36800000, v10
	v_mul_f32_e32 v7, v7, v10
	v_add_f32_e32 v10, 1.0, v11
	v_rcp_f32_e32 v10, v10
	v_mul_f32_e32 v11, 0xbab8aa3b, v13
	v_add_f32_e32 v14, 1.0, v14
	v_exp_f32_e32 v11, v11
	v_rcp_f32_e32 v14, v14
	v_mul_f32_e32 v10, 0x36800000, v10
	v_mul_f32_e32 v8, v8, v10
	v_add_f32_e32 v10, 1.0, v11
	v_mul_f32_e32 v14, 0x36800000, v14
	v_rcp_f32_e32 v10, v10
	v_mul_f32_e32 v105, v105, v109
	v_mul_f32_e32 v65, v65, v69
	v_mul_f32_e32 v49, v49, v53
	v_mul_f32_e32 v6, v6, v14
	v_mul_f32_e32 v119, v121, v122
	v_mul_f32_e32 v103, v105, v106
	v_mul_f32_e32 v97, v97, v101
	v_mul_f32_e32 v81, v81, v85
	v_mul_f32_e32 v63, v65, v66
	v_mul_f32_e32 v57, v57, v61
	v_mul_f32_e32 v47, v49, v50
	v_mul_f32_e32 v41, v41, v45
	v_med3_f32 v6, v6, s23, v179
	v_med3_f32 v7, v7, s23, v179
	v_mov_b32_e32 v11, v3
	v_med3_f32 v128, v128, s23, v179
	v_med3_f32 v126, v129, s23, v179
	v_med3_f32 v120, v120, s23, v179
	v_med3_f32 v119, v119, s23, v179
	v_med3_f32 v104, v104, s23, v179
	v_med3_f32 v103, v103, s23, v179
	v_mul_f32_e32 v95, v97, v98
	v_mul_f32_e32 v89, v89, v93
	v_mul_f32_e32 v79, v81, v82
	v_med3_f32 v64, v64, s23, v179
	v_med3_f32 v63, v63, s23, v179
	v_mul_f32_e32 v55, v57, v58
	v_med3_f32 v48, v48, s23, v179
	v_med3_f32 v47, v47, s23, v179
	v_mul_f32_e32 v39, v41, v42
	v_mul_f32_e32 v33, v33, v37
	v_mul_f32_e32 v17, v17, v21
	v_cvt_pk_fp8_f32 v11, v6, v7
	v_lshrrev_b32_e32 v161, 5, v2
	v_cvt_pk_fp8_f32 v130, v128, v126 op_sel:[0,0,1]
	v_cvt_pk_fp8_f32 v123, v120, v119 op_sel:[0,0,1]
	v_cvt_pk_fp8_f32 v107, v104, v103 op_sel:[0,0,1]
	v_med3_f32 v96, v96, s23, v179
	v_med3_f32 v95, v95, s23, v179
	v_mul_f32_e32 v87, v89, v90
	v_med3_f32 v80, v80, s23, v179
	v_med3_f32 v79, v79, s23, v179
	v_cvt_pk_fp8_f32 v67, v64, v63 op_sel:[0,0,1]
	v_med3_f32 v56, v56, s23, v179
	v_med3_f32 v55, v55, s23, v179
	v_cvt_pk_fp8_f32 v51, v48, v47 op_sel:[0,0,1]
	v_med3_f32 v40, v40, s23, v179
	v_med3_f32 v39, v39, s23, v179
	v_mul_f32_e32 v31, v33, v34
	v_mul_f32_e32 v25, v25, v29
	v_mul_f32_e32 v15, v17, v18
	v_mul_f32_e32 v9, v9, v13
	v_mul_f32_e32 v6, 0x36800000, v10
	v_and_b32_e32 v180, 6, v161
	v_and_b32_e32 v182, 7, v2
	v_cvt_pk_fp8_f32 v99, v96, v95 op_sel:[0,0,1]
	v_med3_f32 v88, v88, s23, v179
	v_med3_f32 v87, v87, s23, v179
	v_cvt_pk_fp8_f32 v83, v80, v79 op_sel:[0,0,1]
	v_cvt_pk_fp8_f32 v59, v56, v55 op_sel:[0,0,1]
	v_cvt_pk_fp8_f32 v43, v40, v39 op_sel:[0,0,1]
	v_med3_f32 v32, v32, s23, v179
	v_med3_f32 v31, v31, s23, v179
	v_mul_f32_e32 v23, v25, v26
	v_med3_f32 v16, v16, s23, v179
	v_med3_f32 v15, v15, s23, v179
	v_mul_f32_e32 v6, v9, v6
	v_bitop3_b32 v126, v161, v182, 6 bitop3:0x6c
	v_bitop3_b32 v110, v180, v182, 1 bitop3:0x36
	v_cvt_pk_fp8_f32 v91, v88, v87 op_sel:[0,0,1]
	v_cvt_pk_fp8_f32 v35, v32, v31 op_sel:[0,0,1]
	v_med3_f32 v24, v24, s23, v179
	v_med3_f32 v23, v23, s23, v179
	v_cvt_pk_fp8_f32 v19, v16, v15 op_sel:[0,0,1]
	v_med3_f32 v8, v8, s23, v179
	v_med3_f32 v6, v6, s23, v179
	v_lshl_add_u32 v126, v126, 4, v157
	v_lshl_add_u32 v110, v110, 4, v157
	v_cvt_pk_fp8_f32 v27, v24, v23 op_sel:[0,0,1]
	v_cvt_pk_fp8_f32 v11, v8, v6 op_sel:[0,0,1]
	ds_write2st64_b32 v126, v130, v115 offset1:8
	ds_write2st64_b32 v110, v123, v107 offset1:8
	ds_write2st64_b32 v126, v99, v83 offset0:16 offset1:24
	ds_write2st64_b32 v110, v91, v75 offset0:16 offset1:24
	ds_write2st64_b32 v126, v67, v51 offset0:32 offset1:40
	ds_write2st64_b32 v110, v59, v43 offset0:32 offset1:40
	ds_write2st64_b32 v126, v35, v19 offset0:48 offset1:56
	ds_write2st64_b32 v110, v27, v11 offset0:48 offset1:56
.LBB0_1063:
	s_or_b64 exec, exec, s[16:17]
	v_xor_b32_e32 v6, v160, v2
	v_lshlrev_b32_e32 v6, 4, v6
	v_and_b32_e32 v18, 0x70, v6
	v_lshlrev_b32_e32 v4, 7, v4
	s_waitcnt lgkmcnt(0)
	s_barrier
	v_add3_u32 v4, v156, v4, v18
	v_lshlrev_b32_e32 v5, 7, v5
	v_add3_u32 v5, v156, v5, v18
	s_waitcnt vmcnt(0)
	v_ashrrev_i32_e32 v163, 31, v162
	v_ashrrev_i32_e32 v159, 31, v158
	v_ashrrev_i32_e32 v167, 31, v166
	v_ashrrev_i32_e32 v165, 31, v164
	ds_read_b128 v[12:15], v4
	ds_read_b128 v[8:11], v5
	v_lshlrev_b32_e32 v4, 7, v181
	v_add3_u32 v4, v156, v4, v18
	s_lshl_b32 s13, s54, 7
	ds_read_b128 v[4:7], v4
	s_ashr_i32 s17, s13, 31
	s_add_u32 s16, s28, s13
	v_lshlrev_b32_e32 v2, 4, v2
	s_addc_u32 s17, s29, s17
	v_and_b32_e32 v2, 0x70, v2
	v_lshl_add_u64 v[16:17], s[16:17], 0, v[2:3]
	v_cmp_lt_i64_e32 vcc, -1, v[162:163]
	s_and_saveexec_b64 s[16:17], vcc
	s_cbranch_execnz .LBB0_1067
	s_or_b64 exec, exec, s[16:17]
	v_cmp_lt_i64_e32 vcc, -1, v[158:159]
	s_and_saveexec_b64 s[16:17], vcc
	s_cbranch_execnz .LBB0_1068
